# expert-weight conversion queue (attention phase): 4 items per claim instead of 8, to shorten the end-of-phase drain tail
# speedup vs baseline: 1.0087x; 1.0087x over previous
; #define RI_NEXT(D_) do { if (q.cnt == 8) { int b_ = 0; if (F.lane == 0) b_ = (int)__hip_atomic_fetch_add(qctr, 8u, __ATOMIC_RELAXED, __HIP_MEMORY_SCOPE_AGENT); q.base = __builtin_amdgcn_readfirstlane(b_); q.cnt = 0; } \
;         D_ = decode_item(KA, F.ws, kind, q.base + q.cnt); ++q.cnt; } while (0)
; DI void run_items1(Frame& F, int kind, int quota, QState& q) {
;     ...
;     if (quota == 0) return;
;     TItem d; RI_NEXT(d); if (!d.valid) return;
; DI void phase_attn(Frame& F, int l) {
;     ...
;     QState cq; cq.base = 0; cq.cnt = 8;
;     constexpr int SLOT_ITEMS = 3;
;     if (F.bid & 1) { __syncthreads(); run_items1(F, 1 + l, SLOT_ITEMS, cq); }
.LBB0_398:
	v_readlane_b32 s8, v255, 14
	v_readlane_b32 s4, v253, 8
	s_lshl_b32 s58, s8, 6
	v_readlane_b32 s6, v253, 10
	v_readlane_b32 s7, v253, 11
	s_lshl_b64 s[0:1], s[58:59], 2
	s_mov_b64 s[2:3], s[6:7]
	s_add_u32 s0, s2, s0
	s_addc_u32 s1, s3, s1
	v_readlane_b32 s9, v255, 15
	s_add_u32 s12, s0, 0x8100
	s_addc_u32 s13, s1, 0
	s_lshl_b64 s[0:1], s[8:9], 25
	v_writelane_b32 v255, s0, 16
	s_lshl_b64 s[62:63], s[8:9], 5
	s_lshl_b32 s2, s8, 20
	v_writelane_b32 v255, s1, 17
	s_mov_b32 s3, s59
	v_readlane_b32 s0, v253, 33
	v_writelane_b32 v255, s2, 18
	s_add_u32 s76, s0, s2
	v_readlane_b32 s0, v253, 34
	v_writelane_b32 v255, s3, 19
	s_addc_u32 s77, s0, 0
	s_lshl_b64 s[20:21], s[8:9], 21
	s_lshl_b64 s[0:1], s[8:9], 20
	v_readlane_b32 s2, v253, 35
	s_add_u32 s22, s2, s0
	v_readlane_b32 s2, v253, 36
	s_addc_u32 s23, s2, s1
	v_readlane_b32 s2, v253, 37
	s_add_u32 s24, s2, s0
	v_readlane_b32 s0, v253, 38
	s_addc_u32 s25, s0, s1
	s_lshl_b64 s[26:27], s[8:9], 24
	v_readlane_b32 s0, v253, 39
	s_add_u32 s14, s0, s44
	v_readlane_b32 s0, v253, 40
	s_addc_u32 s15, s0, s45
	s_mov_b32 s0, -1
	s_mov_b32 s95, 0
	v_mbcnt_lo_u32_b32 v0, s0, 0
	v_mbcnt_hi_u32_b32 v186, s0, v0
	v_readlane_b32 s0, v253, 29
	s_mov_b32 s51, s0
	s_mov_b64 s[30:31], s[70:71]
	s_bitcmp0_b32 s51, 0
	s_mov_b32 s63, 4
	v_readlane_b32 s5, v253, 9
	v_readlane_b32 s1, v253, 30
	s_cbranch_scc1 .LBB0_472
	s_mov_b64 s[6:7], s[70:71]
	v_mov_b32_e32 v0, 0
	v_cmp_eq_u32_e64 s[4:5], 0, v186
	s_waitcnt vmcnt(63) expcnt(7) lgkmcnt(15)
	s_barrier
	s_and_saveexec_b64 s[2:3], s[4:5]
	s_cbranch_execz .LBB0_403
	s_mov_b64 s[10:11], exec
	v_mbcnt_lo_u32_b32 v0, s10, 0
	v_mbcnt_hi_u32_b32 v0, s11, v0
	v_cmp_eq_u32_e32 vcc, 0, v0
	s_and_saveexec_b64 s[8:9], vcc
	s_cbranch_execz .LBB0_402
	s_bcnt1_i32_b64 s0, s[10:11]
	s_lshl_b32 s0, s0, 2
	v_mov_b32_e32 v2, s0
	global_atomic_add v2, v1, v2, s[12:13] sc0
.LBB0_402:
	s_or_b64 exec, exec, s[8:9]
	s_waitcnt vmcnt(0)
	v_readfirstlane_b32 s0, v2
	s_nop 1
	v_lshl_add_u32 v0, v0, 2, s0

; #define LDS_WAIT() asm volatile("s_waitcnt lgkmcnt(0)" ::: "memory")
; #define RI_NEXT(D_) do { if (q.cnt == 8) { int b_ = 0; if (F.lane == 0) b_ = (int)__hip_atomic_fetch_add(qctr, 8u, __ATOMIC_RELAXED, __HIP_MEMORY_SCOPE_AGENT); q.base = __builtin_amdgcn_readfirstlane(b_); q.cnt = 0; } \
;         D_ = decode_item(KA, F.ws, kind, q.base + q.cnt); ++q.cnt; } while (0)
; DI void item_scatter(const f32x4 (&v)[16], LAS float* scr, int lane) {
;     ...
;     for (int i = 0; i < 16; ++i) { const int k = 4 * i + r4;
; #pragma unroll
;         for (int j = 0; j < 4; ++j) scr[(4 * c4 + j) * 64 + (k ^ (4 * (c4 ^ j)))] = v[i][j]; }
;     LDS_WAIT(); asm volatile("" ::: "memory");
; DI void run_items1(Frame& F, int kind, int quota, QState& q) {
;     ...
;         item_scatter(v, scr, F.lane);
;         TItem dn; dn.valid = false;
;         if (quota < 0 || n < quota) { RI_NEXT(dn); if (dn.valid) item_load(dn, v, F.lane); }
.LBB0_430:
	s_waitcnt vmcnt(0)
	ds_write_b32 v93, v2
	ds_write_b32 v94, v3 offset:256
	ds_write_b32 v95, v4 offset:512
	ds_write_b32 v96, v5 offset:768
	ds_write_b32 v97, v6
	ds_write_b32 v98, v7 offset:256
	ds_write_b32 v99, v8 offset:512
	ds_write_b32 v100, v9 offset:768
	ds_write_b32 v101, v10
	ds_write_b32 v102, v11 offset:256
	ds_write_b32 v103, v12 offset:512
	ds_write_b32 v104, v13 offset:768
	ds_write_b32 v105, v14
	ds_write_b32 v106, v15 offset:256
	ds_write_b32 v107, v16 offset:512
	ds_write_b32 v108, v17 offset:768
	ds_write_b32 v109, v18
	ds_write_b32 v110, v19 offset:256
	ds_write_b32 v111, v20 offset:512
	ds_write_b32 v112, v21 offset:768
	ds_write_b32 v113, v22
	ds_write_b32 v114, v23 offset:256
	ds_write_b32 v115, v24 offset:512
	ds_write_b32 v116, v25 offset:768
	ds_write_b32 v117, v26
	ds_write_b32 v118, v27 offset:256
	ds_write_b32 v119, v28 offset:512
	ds_write_b32 v120, v29 offset:768
	ds_write_b32 v121, v30
	ds_write_b32 v122, v31 offset:256
	ds_write_b32 v123, v32 offset:512
	ds_write_b32 v124, v33 offset:768
	ds_write_b32 v125, v34
	ds_write_b32 v126, v35 offset:256
	ds_write_b32 v127, v36 offset:512
	ds_write_b32 v128, v37 offset:768
	ds_write_b32 v129, v38
	ds_write_b32 v130, v39 offset:256
	ds_write_b32 v131, v40 offset:512
	ds_write_b32 v132, v41 offset:768
	ds_write_b32 v133, v42
	ds_write_b32 v134, v43 offset:256
	ds_write_b32 v135, v44 offset:512
	ds_write_b32 v136, v45 offset:768
	ds_write_b32 v137, v46
	ds_write_b32 v138, v47 offset:256
	ds_write_b32 v139, v48 offset:512
	ds_write_b32 v140, v49 offset:768
	ds_write_b32 v141, v50
	ds_write_b32 v142, v51 offset:256
	ds_write_b32 v143, v52 offset:512
	ds_write_b32 v144, v53 offset:768
	ds_write_b32 v145, v54
	ds_write_b32 v146, v55 offset:256
	ds_write_b32 v147, v56 offset:512
	ds_write_b32 v148, v57 offset:768
	ds_write_b32 v149, v58
	ds_write_b32 v150, v59 offset:256
	ds_write_b32 v151, v60 offset:512
	ds_write_b32 v152, v61 offset:768
	ds_write_b32 v153, v62
	ds_write_b32 v154, v63 offset:256
	ds_write_b32 v155, v64 offset:512
	ds_write_b32 v156, v65 offset:768
	s_waitcnt lgkmcnt(0)
	s_cmp_gt_u32 s38, 2
	s_mov_b64 s[2:3], 0
	s_cbranch_scc1 .LBB0_465
	s_cmp_lg_u32 s63, 4
	s_cbranch_scc1 .LBB0_437
	v_mov_b32_e32 v0, 0
	s_and_saveexec_b64 s[2:3], s[4:5]
	s_cbranch_execz .LBB0_436
	s_mov_b64 s[18:19], exec
	v_mbcnt_lo_u32_b32 v0, s18, 0
	v_mbcnt_hi_u32_b32 v0, s19, v0
	v_cmp_eq_u32_e32 vcc, 0, v0
	s_and_saveexec_b64 s[16:17], vcc
	s_cbranch_execz .LBB0_435
	s_bcnt1_i32_b64 s0, s[18:19]
	s_lshl_b32 s0, s0, 2
	v_mov_b32_e32 v66, s0
	global_atomic_add v66, v1, v66, s[12:13] sc0
.LBB0_435:
	s_or_b64 exec, exec, s[16:17]
	s_waitcnt vmcnt(0)
	v_readfirstlane_b32 s0, v66
	s_nop 1
	v_lshl_add_u32 v0, v0, 2, s0

; DI unsigned pk4_fp8(float a, float b, float c, float d) { int r = 0; r = __builtin_amdgcn_cvt_pk_fp8_f32(sat8(a), sat8(b), r, false); r = __builtin_amdgcn_cvt_pk_fp8_f32(sat8(c), sat8(d), r, true); return (unsigned)r; }
; DI float half_sum(float v) { const auto rr = __builtin_amdgcn_permlane32_swap(__float_as_uint(v), __float_as_uint(v), false, false); return __uint_as_float(rr[0]) + __uint_as_float(rr[1]); }
; DI void phase_attn(Frame& F, int l) {
;     ...
;         const float ltot = half_sum(l_run); const float inv = AZ8_SCALE / ltot;
; #pragma unroll
;         for (int ds = 0; ds < 2; ++ds)
; #pragma unroll
;             for (int g4 = 0; g4 < 4; g4 += 2) {
;                 const unsigned wa = pk4_fp8(o[ds][4 * g4] * inv, o[ds][4 * g4 + 1] * inv, o[ds][4 * g4 + 2] * inv, o[ds][4 * g4 + 3] * inv), wb = pk4_fp8(o[ds][4 * g4 + 4] * inv, o[ds][4 * g4 + 5] * inv, o[ds][4 * g4 + 6] * inv, o[ds][4 * g4 + 7] * inv);
;                 const auto rr = __builtin_amdgcn_permlane32_swap(wa, wb, false, false);
;                 u32x2 w; w.x = rr[0]; w.y = rr[1];
;                 *(u32x2*)(att + qtok * D + h * HD + 32 * ds + 8 * (g4 + hh)) = w; }
;         if (!((F.bid & 1) && it == 3)) { __syncthreads(); run_items1(F, 1 + l, SLOT_ITEMS, cq); }
.LBB0_568:
	v_mov_b32_e32 v0, v11
	s_nop 1
	v_permlane32_swap_b32_e32 v11, v0
	v_add_f32_e32 v0, v11, v0
	s_mov_b32 s2, 0x41000000
	s_waitcnt vmcnt(1)
	v_div_scale_f32 v2, s[0:1], v0, v0, s2
	v_rcp_f32_e32 v3, v2
	v_readlane_b32 s0, v253, 21
	v_readlane_b32 s1, v253, 22
	s_bitcmp1_b32 s19, 0
	v_fma_f32 v4, -v2, v3, 1.0
	v_fmac_f32_e32 v3, v4, v3
	v_div_scale_f32 v4, vcc, s2, v0, s2
	v_mul_f32_e32 v5, v4, v3
	s_waitcnt vmcnt(0)
	v_fma_f32 v6, -v2, v5, v4
	v_fmac_f32_e32 v5, v6, v3
	v_fma_f32 v2, -v2, v5, v4
	v_div_fmas_f32 v2, v2, v3, v5
	v_div_fixup_f32 v0, v2, v0, s2
	v_mul_f32_e32 v2, v16, v0
	v_mul_f32_e32 v3, v17, v0
	v_med3_f32 v5, v2, s53, v204
	v_med3_f32 v3, v3, s53, v204
	v_mov_b32_e32 v2, v1
	v_cvt_pk_fp8_f32 v2, v5, v3
	v_mul_f32_e32 v4, v18, v0
	v_mul_f32_e32 v3, v19, v0
	v_med3_f32 v4, v4, s53, v204
	v_med3_f32 v3, v3, s53, v204
	v_cvt_pk_fp8_f32 v2, v4, v3 op_sel:[0,0,1]
	v_mul_f32_e32 v3, v20, v0
	v_mul_f32_e32 v4, v21, v0
	v_med3_f32 v6, v3, s53, v204
	v_med3_f32 v4, v4, s53, v204
	v_mov_b32_e32 v3, v1
	v_cvt_pk_fp8_f32 v3, v6, v4
	v_mul_f32_e32 v6, v24, v0
	v_mul_f32_e32 v7, v25, v0
	v_med3_f32 v9, v6, s53, v204
	v_med3_f32 v7, v7, s53, v204
	v_mov_b32_e32 v6, v1
	v_cvt_pk_fp8_f32 v6, v9, v7
	v_mul_f32_e32 v8, v26, v0
	v_mul_f32_e32 v7, v27, v0
	v_med3_f32 v8, v8, s53, v204
	v_med3_f32 v7, v7, s53, v204
	v_cvt_pk_fp8_f32 v6, v8, v7 op_sel:[0,0,1]
	v_mul_f32_e32 v7, v28, v0
	v_mul_f32_e32 v8, v29, v0
	v_med3_f32 v10, v7, s53, v204
	v_med3_f32 v8, v8, s53, v204
	v_mov_b32_e32 v7, v1
	v_cvt_pk_fp8_f32 v7, v10, v8
	v_mul_f32_e32 v5, v22, v0
	v_mul_f32_e32 v4, v23, v0
	v_med3_f32 v5, v5, s53, v204
	v_med3_f32 v4, v4, s53, v204
	v_mul_f32_e32 v9, v30, v0
	v_mul_f32_e32 v8, v31, v0
	v_cvt_pk_fp8_f32 v3, v5, v4 op_sel:[0,0,1]
	v_med3_f32 v9, v9, s53, v204
	v_med3_f32 v8, v8, s53, v204
	v_cvt_pk_fp8_f32 v7, v9, v8 op_sel:[0,0,1]
	v_lshl_add_u64 v[4:5], s[0:1], 0, v[170:171]
	v_lshl_add_u64 v[4:5], v[4:5], 0, s[58:59]
	v_permlane32_swap_b32_e32 v2, v3
	v_lshl_add_u64 v[4:5], v[4:5], 0, v[168:169]
	global_store_dwordx2 v[4:5], v[2:3], off
	v_permlane32_swap_b32_e32 v6, v7
	v_mul_f32_e32 v2, v32, v0
	v_mul_f32_e32 v3, v33, v0
	global_store_dwordx2 v[4:5], v[6:7], off offset:16
	v_med3_f32 v7, v2, s53, v204
	v_med3_f32 v3, v3, s53, v204
	v_mov_b32_e32 v2, v1
	v_cvt_pk_fp8_f32 v2, v7, v3
	v_mul_f32_e32 v6, v34, v0
	v_mul_f32_e32 v3, v35, v0
	v_med3_f32 v6, v6, s53, v204
	v_med3_f32 v3, v3, s53, v204
	v_cvt_pk_fp8_f32 v2, v6, v3 op_sel:[0,0,1]
	v_mul_f32_e32 v3, v36, v0
	v_mul_f32_e32 v6, v37, v0
	v_med3_f32 v8, v3, s53, v204
	v_med3_f32 v6, v6, s53, v204
	v_mov_b32_e32 v3, v1
	v_cvt_pk_fp8_f32 v3, v8, v6
	v_mul_f32_e32 v7, v38, v0
	v_mul_f32_e32 v6, v39, v0
	v_med3_f32 v7, v7, s53, v204
	v_med3_f32 v6, v6, s53, v204
	v_cvt_pk_fp8_f32 v3, v7, v6 op_sel:[0,0,1]
	v_mul_f32_e32 v6, v40, v0
	v_mul_f32_e32 v7, v41, v0
	v_med3_f32 v9, v6, s53, v204
	v_med3_f32 v7, v7, s53, v204
	v_mov_b32_e32 v6, v1
	v_cvt_pk_fp8_f32 v6, v9, v7
	v_mul_f32_e32 v8, v42, v0
	v_mul_f32_e32 v7, v43, v0
	v_med3_f32 v8, v8, s53, v204
	v_med3_f32 v7, v7, s53, v204
	v_cvt_pk_fp8_f32 v6, v8, v7 op_sel:[0,0,1]
	v_mul_f32_e32 v7, v44, v0
	v_mul_f32_e32 v8, v45, v0
	v_med3_f32 v10, v7, s53, v204
	v_med3_f32 v8, v8, s53, v204
	v_mov_b32_e32 v7, v1
	v_cvt_pk_fp8_f32 v7, v10, v8
	v_mul_f32_e32 v9, v46, v0
	v_mul_f32_e32 v0, v47, v0
	v_med3_f32 v8, v9, s53, v204
	v_med3_f32 v0, v0, s53, v204
	v_cvt_pk_fp8_f32 v7, v8, v0 op_sel:[0,0,1]
	s_cselect_b64 s[0:1], -1, 0
	s_cmp_eq_u32 s18, 3
	s_cselect_b64 s[2:3], -1, 0
	s_and_b64 s[0:1], s[2:3], s[0:1]
	v_permlane32_swap_b32_e32 v2, v3
	v_permlane32_swap_b32_e32 v6, v7
	s_and_b64 vcc, exec, s[0:1]
	global_store_dwordx2 v[4:5], v[2:3], off offset:32
	global_store_dwordx2 v[4:5], v[6:7], off offset:48
	s_cbranch_vccnz .LBB0_474
	s_mov_b64 s[6:7], s[70:71]
	s_cmp_lg_u32 s63, 4
	s_barrier
	s_cbranch_scc1 .LBB0_575
	v_mov_b32_e32 v0, 0
	s_and_saveexec_b64 s[2:3], s[4:5]
	s_cbranch_execz .LBB0_574
	s_mov_b64 s[10:11], exec
	v_mbcnt_lo_u32_b32 v0, s10, 0
	v_mbcnt_hi_u32_b32 v0, s11, v0
	v_cmp_eq_u32_e32 vcc, 0, v0
	s_and_saveexec_b64 s[8:9], vcc
	s_cbranch_execz .LBB0_573
	s_bcnt1_i32_b64 s0, s[10:11]
	s_lshl_b32 s0, s0, 2
	v_mov_b32_e32 v2, s0
	global_atomic_add v2, v1, v2, s[12:13] sc0

; #define LDS_WAIT() asm volatile("s_waitcnt lgkmcnt(0)" ::: "memory")
; #define RI_NEXT(D_) do { if (q.cnt == 8) { int b_ = 0; if (F.lane == 0) b_ = (int)__hip_atomic_fetch_add(qctr, 8u, __ATOMIC_RELAXED, __HIP_MEMORY_SCOPE_AGENT); q.base = __builtin_amdgcn_readfirstlane(b_); q.cnt = 0; } \
;         D_ = decode_item(KA, F.ws, kind, q.base + q.cnt); ++q.cnt; } while (0)
; DI void item_scatter(const f32x4 (&v)[16], LAS float* scr, int lane) {
;     ...
;     for (int i = 0; i < 16; ++i) { const int k = 4 * i + r4;
; #pragma unroll
;         for (int j = 0; j < 4; ++j) scr[(4 * c4 + j) * 64 + (k ^ (4 * (c4 ^ j)))] = v[i][j]; }
;     LDS_WAIT(); asm volatile("" ::: "memory");
; DI void run_items1(Frame& F, int kind, int quota, QState& q) {
;     ...
;         item_scatter(v, scr, F.lane);
;         TItem dn; dn.valid = false;
;         if (quota < 0 || n < quota) { RI_NEXT(dn); if (dn.valid) item_load(dn, v, F.lane); }
.LBB0_602:
	s_waitcnt vmcnt(15)
	ds_write_b32 v93, v2
	ds_write_b32 v94, v3 offset:256
	ds_write_b32 v95, v4 offset:512
	ds_write_b32 v96, v5 offset:768
	s_waitcnt vmcnt(14)
	ds_write_b32 v97, v6
	ds_write_b32 v98, v7 offset:256
	ds_write_b32 v99, v8 offset:512
	ds_write_b32 v100, v9 offset:768
	s_waitcnt vmcnt(13)
	ds_write_b32 v101, v10
	ds_write_b32 v102, v11 offset:256
	ds_write_b32 v103, v12 offset:512
	ds_write_b32 v104, v13 offset:768
	s_waitcnt vmcnt(12)
	ds_write_b32 v105, v14
	ds_write_b32 v106, v15 offset:256
	ds_write_b32 v107, v16 offset:512
	ds_write_b32 v108, v17 offset:768
	s_waitcnt vmcnt(11)
	ds_write_b32 v109, v18
	ds_write_b32 v110, v19 offset:256
	ds_write_b32 v111, v20 offset:512
	ds_write_b32 v112, v21 offset:768
	s_waitcnt vmcnt(10)
	ds_write_b32 v113, v22
	ds_write_b32 v114, v23 offset:256
	ds_write_b32 v115, v24 offset:512
	ds_write_b32 v116, v25 offset:768
	s_waitcnt vmcnt(9)
	ds_write_b32 v117, v26
	ds_write_b32 v118, v27 offset:256
	ds_write_b32 v119, v28 offset:512
	ds_write_b32 v120, v29 offset:768
	s_waitcnt vmcnt(8)
	ds_write_b32 v121, v30
	ds_write_b32 v122, v31 offset:256
	ds_write_b32 v123, v32 offset:512
	ds_write_b32 v124, v33 offset:768
	s_waitcnt vmcnt(7)
	ds_write_b32 v125, v34
	ds_write_b32 v126, v35 offset:256
	ds_write_b32 v127, v36 offset:512
	ds_write_b32 v128, v37 offset:768
	s_waitcnt vmcnt(6)
	ds_write_b32 v129, v38
	ds_write_b32 v130, v39 offset:256
	ds_write_b32 v131, v40 offset:512
	ds_write_b32 v132, v41 offset:768
	s_waitcnt vmcnt(5)
	ds_write_b32 v133, v42
	ds_write_b32 v134, v43 offset:256
	ds_write_b32 v135, v44 offset:512
	ds_write_b32 v136, v45 offset:768
	s_waitcnt vmcnt(4)
	ds_write_b32 v137, v46
	ds_write_b32 v138, v47 offset:256
	ds_write_b32 v139, v48 offset:512
	ds_write_b32 v140, v49 offset:768
	s_waitcnt vmcnt(3)
	ds_write_b32 v141, v50
	ds_write_b32 v142, v51 offset:256
	ds_write_b32 v143, v52 offset:512
	ds_write_b32 v144, v53 offset:768
	s_waitcnt vmcnt(2)
	ds_write_b32 v145, v54
	ds_write_b32 v146, v55 offset:256
	ds_write_b32 v147, v56 offset:512
	ds_write_b32 v148, v57 offset:768
	s_waitcnt vmcnt(1)
	ds_write_b32 v149, v58
	ds_write_b32 v150, v59 offset:256
	ds_write_b32 v151, v60 offset:512
	ds_write_b32 v152, v61 offset:768
	s_waitcnt vmcnt(0)
	ds_write_b32 v153, v62
	ds_write_b32 v154, v63 offset:256
	ds_write_b32 v155, v64 offset:512
	ds_write_b32 v156, v65 offset:768
	s_waitcnt lgkmcnt(0)
	s_cmp_gt_u32 s38, 2
	s_mov_b64 s[2:3], 0
	s_cbranch_scc1 .LBB0_637
	s_cmp_lg_u32 s63, 4
	s_cbranch_scc1 .LBB0_609
	v_mov_b32_e32 v0, 0
	s_and_saveexec_b64 s[2:3], s[4:5]
	s_cbranch_execz .LBB0_608
	s_mov_b64 s[18:19], exec
	v_mbcnt_lo_u32_b32 v0, s18, 0
	v_mbcnt_hi_u32_b32 v0, s19, v0
	v_cmp_eq_u32_e32 vcc, 0, v0
	s_and_saveexec_b64 s[16:17], vcc
	s_cbranch_execz .LBB0_607
	s_bcnt1_i32_b64 s0, s[18:19]
	s_lshl_b32 s0, s0, 2
	v_mov_b32_e32 v66, s0
	global_atomic_add v66, v1, v66, s[12:13] sc0

; DI void phase_attn(Frame& F, int l) {
;     ...
;     __syncthreads();
;     run_items1(F, 1 + l, -1, cq);
.LBB0_645:
	s_mov_b64 s[6:7], s[70:71]
	s_cmp_lg_u32 s63, 4
	s_waitcnt lgkmcnt(0)
	s_barrier
	s_cbranch_scc1 .LBB0_651
	v_mov_b32_e32 v0, 0
	v_cmp_eq_u32_e32 vcc, 0, v186
	s_and_saveexec_b64 s[2:3], vcc
	s_cbranch_execz .LBB0_650
	s_mov_b64 s[8:9], exec
	v_mbcnt_lo_u32_b32 v0, s8, 0
	v_mbcnt_hi_u32_b32 v0, s9, v0
	v_cmp_eq_u32_e32 vcc, 0, v0
	s_and_saveexec_b64 s[4:5], vcc
	s_cbranch_execz .LBB0_649
	s_bcnt1_i32_b64 s0, s[8:9]
	s_lshl_b32 s0, s0, 2
	s_waitcnt vmcnt(0)
	v_mov_b32_e32 v2, s0
	global_atomic_add v2, v1, v2, s[12:13] sc0
.LBB0_649:
	s_or_b64 exec, exec, s[4:5]
	s_waitcnt vmcnt(0)
	v_readfirstlane_b32 s0, v2
	s_nop 1
	v_lshl_add_u32 v0, v0, 2, s0

; #define LDS_WAIT() asm volatile("s_waitcnt lgkmcnt(0)" ::: "memory")
; #define RI_NEXT(D_) do { if (q.cnt == 8) { int b_ = 0; if (F.lane == 0) b_ = (int)__hip_atomic_fetch_add(qctr, 8u, __ATOMIC_RELAXED, __HIP_MEMORY_SCOPE_AGENT); q.base = __builtin_amdgcn_readfirstlane(b_); q.cnt = 0; } \
;         D_ = decode_item(KA, F.ws, kind, q.base + q.cnt); ++q.cnt; } while (0)
; DI void item_scatter(const f32x4 (&v)[16], LAS float* scr, int lane) {
;     ...
;     for (int i = 0; i < 16; ++i) { const int k = 4 * i + r4;
; #pragma unroll
;         for (int j = 0; j < 4; ++j) scr[(4 * c4 + j) * 64 + (k ^ (4 * (c4 ^ j)))] = v[i][j]; }
;     LDS_WAIT(); asm volatile("" ::: "memory");
; DI void run_items1(Frame& F, int kind, int quota, QState& q) {
;     ...
;     for (int n = 1; ; ++n) {
;         item_scatter(v, scr, F.lane);
;         TItem dn; dn.valid = false;
;         if (quota < 0 || n < quota) { RI_NEXT(dn); if (dn.valid) item_load(dn, v, F.lane); }
.LBB0_678:
	s_waitcnt vmcnt(15)
	ds_write_b32 v93, v2
	ds_write_b32 v94, v3 offset:256
	ds_write_b32 v95, v4 offset:512
	ds_write_b32 v96, v5 offset:768
	s_waitcnt vmcnt(14)
	ds_write_b32 v97, v6
	ds_write_b32 v98, v7 offset:256
	ds_write_b32 v99, v8 offset:512
	ds_write_b32 v100, v9 offset:768
	s_waitcnt vmcnt(13)
	ds_write_b32 v101, v10
	ds_write_b32 v102, v11 offset:256
	ds_write_b32 v103, v12 offset:512
	ds_write_b32 v104, v13 offset:768
	s_waitcnt vmcnt(12)
	ds_write_b32 v105, v14
	ds_write_b32 v106, v15 offset:256
	ds_write_b32 v107, v16 offset:512
	ds_write_b32 v108, v17 offset:768
	s_waitcnt vmcnt(11)
	ds_write_b32 v109, v18
	ds_write_b32 v110, v19 offset:256
	ds_write_b32 v111, v20 offset:512
	ds_write_b32 v112, v21 offset:768
	s_waitcnt vmcnt(10)
	ds_write_b32 v113, v22
	ds_write_b32 v114, v23 offset:256
	ds_write_b32 v115, v24 offset:512
	ds_write_b32 v116, v25 offset:768
	s_waitcnt vmcnt(9)
	ds_write_b32 v117, v26
	ds_write_b32 v118, v27 offset:256
	ds_write_b32 v119, v28 offset:512
	ds_write_b32 v120, v29 offset:768
	s_waitcnt vmcnt(8)
	ds_write_b32 v121, v30
	ds_write_b32 v122, v31 offset:256
	ds_write_b32 v123, v32 offset:512
	ds_write_b32 v124, v33 offset:768
	s_waitcnt vmcnt(7)
	ds_write_b32 v125, v34
	ds_write_b32 v126, v35 offset:256
	ds_write_b32 v127, v36 offset:512
	ds_write_b32 v128, v37 offset:768
	s_waitcnt vmcnt(6)
	ds_write_b32 v129, v38
	ds_write_b32 v130, v39 offset:256
	ds_write_b32 v131, v40 offset:512
	ds_write_b32 v132, v41 offset:768
	s_waitcnt vmcnt(5)
	ds_write_b32 v133, v42
	ds_write_b32 v134, v43 offset:256
	ds_write_b32 v135, v44 offset:512
	ds_write_b32 v136, v45 offset:768
	s_waitcnt vmcnt(4)
	ds_write_b32 v137, v46
	ds_write_b32 v138, v47 offset:256
	ds_write_b32 v139, v48 offset:512
	ds_write_b32 v140, v49 offset:768
	s_waitcnt vmcnt(3)
	ds_write_b32 v141, v50
	ds_write_b32 v142, v51 offset:256
	ds_write_b32 v143, v52 offset:512
	ds_write_b32 v144, v53 offset:768
	s_waitcnt vmcnt(2)
	ds_write_b32 v145, v54
	ds_write_b32 v146, v55 offset:256
	ds_write_b32 v147, v56 offset:512
	ds_write_b32 v148, v57 offset:768
	s_waitcnt vmcnt(1)
	ds_write_b32 v149, v58
	ds_write_b32 v150, v59 offset:256
	ds_write_b32 v151, v60 offset:512
	ds_write_b32 v152, v61 offset:768
	s_waitcnt vmcnt(0)
	ds_write_b32 v153, v62
	ds_write_b32 v154, v63 offset:256
	ds_write_b32 v155, v64 offset:512
	ds_write_b32 v156, v65 offset:768
	s_waitcnt lgkmcnt(0)
	s_add_i32 s63, s63, 1
	s_cmp_lg_u32 s63, 4
	s_cbranch_scc1 .LBB0_684
	v_mov_b32_e32 v0, 0
	s_and_saveexec_b64 s[2:3], s[4:5]
	s_cbranch_execz .LBB0_683
	s_mov_b64 s[18:19], exec
	v_mbcnt_lo_u32_b32 v0, s18, 0
	v_mbcnt_hi_u32_b32 v0, s19, v0
	v_cmp_eq_u32_e32 vcc, 0, v0
	s_and_saveexec_b64 s[16:17], vcc
	s_cbranch_execz .LBB0_682
	s_bcnt1_i32_b64 s0, s[18:19]
	s_lshl_b32 s0, s0, 2
	v_mov_b32_e32 v66, s0
	global_atomic_add v66, v1, v66, s[12:13] sc0
